# masked attention step: tile j+2 staging (LDS-DMA + mask words) issued behind the QK^T matrix ops instead of in front of the step's LDS reads
# baseline (speedup 1.0000x reference)
; #define LAS __attribute__((address_space(3)))
; __device__ __forceinline__ void dsa_qk(f32x16& p0, f32x16& p1, const LAS char* kp, const bf16x8 (&qr)[4], unsigned long long mw, int hi, float mref, const LAS char* tbl) {
;     bf16x8 kf[8];
; #pragma unroll
;     for (int d0 = 0; d0 < 4; ++d0) { kf[2 * d0] = *(const LAS bf16x8*)(kp + d0 * 2048); kf[2 * d0 + 1] = *(const LAS bf16x8*)(kp + d0 * 2048 + 512); }
;     const unsigned mlo = (unsigned)mw >> (4 * hi), mhi = (unsigned)(mw >> 32) >> (4 * hi), negm = __float_as_uint(-mref);
;     if (tbl) {
; #pragma unroll
;         for (int i = 0; i < 4; ++i) { const u32x4 a = *(const LAS u32x4*)(tbl + ((mlo >> (8 * i)) & 15u) * 16u), b = *(const LAS u32x4*)(tbl + ((mhi >> (8 * i)) & 15u) * 16u);
; #pragma unroll
;             for (int e = 0; e < 4; ++e) { p0[4 * i + e] = __uint_as_float(a[e]); p1[4 * i + e] = __uint_as_float(b[e]); } }
; __device__ __forceinline__ void dsa_block_unit(int b, int g, int m  , const bf16_t* Q, const bf16_t* K, const bf16_t* V, const unsigned long long* mask, bf16_t* O, LAS char* L, int wid, int lane, float sbound  ) {
;     ...
;     for (int j = 0; j <= jd; j += 2) {
;         if (j + 2 <= jd) { glds16_s(Kw + (size_t)(j + 2) * 64 * 128, kvoff, kdst + sn2); glds16_s(Vw + (size_t)(j + 2) * 64 * 128, vvoff, vdst + sn2); mwn2 = mrow[j + 2]; }
.LBB0_1684:
	s_add_i32 s60, s58, -1
	s_mov_b32 s59, s0
	s_cmp_gt_u32 s60, s54
	s_waitcnt vmcnt(0)
	v_mov_b64_e32 v[170:171], v[116:117]
.LBB0_1686:
	s_add_i32 s0, s58, -3
	s_cmp_lt_u32 s0, s54
	s_cselect_b64 s[34:35], -1, 0
	s_cmp_ge_u32 s0, s54
	s_cbranch_scc1 .LBB0_1692
	v_add_u32_e32 v66, s57, v174
	ds_read_b128 v[146:149], v66
	ds_read_b128 v[142:145], v66 offset:512
	ds_read_b128 v[138:141], v66 offset:2048
	ds_read_b128 v[134:137], v66 offset:2560
	ds_read_b128 v[130:133], v66 offset:4096
	ds_read_b128 v[126:129], v66 offset:4608
	ds_read_b128 v[122:125], v66 offset:6144
	ds_read_b128 v[118:121], v66 offset:6656
	v_lshrrev_b32_e32 v115, v176, v116
	v_lshrrev_b32_e32 v114, v176, v117
	s_and_saveexec_b64 s[0:1], s[4:5]
	s_xor_b64 s[36:37], exec, s[0:1]
	s_cbranch_execz .LBB0_1689
	v_lshlrev_b32_e32 v66, 4, v115
	v_lshlrev_b32_e32 v67, 4, v114
	v_lshrrev_b32_e32 v70, 4, v115
	v_lshrrev_b32_e32 v71, 4, v114
	v_lshrrev_b32_e32 v74, 12, v115
	v_lshrrev_b32_e32 v75, 12, v114
	v_lshrrev_b32_e32 v78, 20, v115
	v_lshrrev_b32_e32 v79, 20, v114
	s_add_i32 s0, 0, 0x14800
	v_mov_b32_e32 v206, 0xf0
	v_and_or_b32 v66, v66, v206, s0
	v_and_or_b32 v67, v67, v206, s0
	v_and_or_b32 v70, v70, v206, s0
	v_and_or_b32 v71, v71, v206, s0
	v_and_or_b32 v74, v74, v206, s0
	v_and_or_b32 v75, v75, v206, s0
	v_and_or_b32 v78, v78, v206, s0
	v_and_or_b32 v79, v79, v206, s0
	ds_read_b128 v[82:85], v66
	ds_read_b128 v[66:69], v67
	ds_read_b128 v[86:89], v70
	ds_read_b128 v[70:73], v71
	ds_read_b128 v[90:93], v74
	ds_read_b128 v[74:77], v75
	ds_read_b128 v[94:97], v78
	ds_read_b128 v[78:81], v79

; #define LAS __attribute__((address_space(3)))
; __device__ __forceinline__ float max3f(float a, float b, float c) { float r; asm("v_max3_f32 %0, %1, %2, %3" : "=v"(r) : "v"(a), "v"(b), "v"(c)); return r; }
; __device__ __forceinline__ void dsa_qk(f32x16& p0, f32x16& p1, const LAS char* kp, const bf16x8 (&qr)[4], unsigned long long mw, int hi, float mref, const LAS char* tbl) {
;     ...
; #pragma unroll
;     for (int d0 = 0; d0 < 4; ++d0) {
;         p0 = __builtin_amdgcn_mfma_f32_32x32x16_bf16(kf[2 * d0], qr[d0], p0, 0, 0, 0);
;         p1 = __builtin_amdgcn_mfma_f32_32x32x16_bf16(kf[2 * d0 + 1], qr[d0], p1, 0, 0, 0);
;     }
; }
; __device__ __forceinline__ void dsa_step(f32x16& c0, f32x16& c1, f32x16& n0, f32x16& n1, const bool have_n, const LAS char* kpn, const LAS char* vpc, const bf16x8 (&qr)[4], unsigned long long mwn, ...
;     if (have_n) dsa_qk(n0, n1, kpn, qr, mwn, hi, mref, fixed ? tblp : (const LAS char*)nullptr);
;     bf16x8 vf[8]; pv_load(vf, vpc);
;     __builtin_amdgcn_sched_barrier(0);
;     bool resc = false; float rm = 0.f;
;     if (!fixed) {
;         rm = __builtin_fmaxf(c0[0], c1[0]);
; #pragma unroll
;         for (int r = 1; r < 16; ++r) rm = max3f(rm, c0[r], c1[r]);
;         rm = __builtin_fmaxf(rm, swap_other(rm, hi));
;         resc = __builtin_amdgcn_ballot_w64(rm > DSA_THR) != 0ull;
; __device__ __forceinline__ void dsa_block_unit(int b, int g, int m  , const bf16_t* Q, const bf16_t* K, const bf16_t* V, const unsigned long long* mask, bf16_t* O, LAS char* L, int wid, int lane, float sbound  ) {
;     ...
;         if (j + 2 <= jd) { glds16_s(Kw + (size_t)(j + 2) * 64 * 128, kvoff, kdst + sn2); glds16_s(Vw + (size_t)(j + 2) * 64 * 128, vvoff, vdst + sn2); mwn2 = mrow[j + 2]; }
.LBB0_1691:
	s_or_b64 exec, exec, s[36:37]
	s_waitcnt lgkmcnt(1)
	v_mfma_f32_32x32x16_bf16 v[82:97], v[146:149], v[98:101], v[82:97]
	s_waitcnt lgkmcnt(0)
	v_mfma_f32_32x32x16_bf16 v[66:81], v[142:145], v[98:101], v[66:81]
	v_mfma_f32_32x32x16_bf16 v[82:97], v[138:141], v[102:105], v[82:97]
	v_mfma_f32_32x32x16_bf16 v[66:81], v[134:137], v[102:105], v[66:81]
	v_mfma_f32_32x32x16_bf16 v[82:97], v[130:133], v[106:109], v[82:97]
	v_mfma_f32_32x32x16_bf16 v[66:81], v[126:129], v[106:109], v[66:81]
	v_mfma_f32_32x32x16_bf16 v[82:97], v[122:125], v[110:113], v[82:97]
	v_mfma_f32_32x32x16_bf16 v[66:81], v[118:121], v[110:113], v[66:81]
	s_cmp_gt_u32 s60, s54
	s_cbranch_scc1 .Ldl0_skip
	s_add_u32 s0, s16, s30
	s_addc_u32 s1, s17, s31
	s_add_u32 s0, s0, 0x8000
	s_addc_u32 s1, s1, 0
	s_add_i32 s33, s59, s63
	s_add_u32 s2, s18, s30
	s_addc_u32 s3, s19, s31
	s_add_u32 s2, s2, 0x8000
	s_mov_b32 s101, m0
	s_mov_b32 m0, s33
	s_nop 0
	global_load_lds_dwordx4 v172, s[0:1]
	s_mov_b32 m0, s101
	s_addc_u32 s3, s3, 0
	s_add_i32 s100, s59, s64
	s_mov_b32 s0, m0
	s_mov_b32 m0, s100
	s_nop 0
	global_load_lds_dwordx4 v173, s[2:3]
	s_mov_b32 m0, s0
	global_load_dwordx2 v[170:171], v[168:169], off offset:-8 sc1
.Ldl0_skip:
.LBB0_1692:
	v_add_u32_e32 v116, s55, v175
	ds_read_b64_tr_b16 v[142:143], v116 offset:24576
	ds_read_b64_tr_b16 v[144:145], v116 offset:25088
	ds_read_b64_tr_b16 v[134:135], v116 offset:25600
	ds_read_b64_tr_b16 v[136:137], v116 offset:26112
	ds_read_b64_tr_b16 v[138:139], v116 offset:28672
	ds_read_b64_tr_b16 v[140:141], v116 offset:29184
	ds_read_b64_tr_b16 v[130:131], v116 offset:29696
	ds_read_b64_tr_b16 v[132:133], v116 offset:30208
	ds_read_b64_tr_b16 v[126:127], v116 offset:26624
	ds_read_b64_tr_b16 v[128:129], v116 offset:27136
	ds_read_b64_tr_b16 v[118:119], v116 offset:27648
	ds_read_b64_tr_b16 v[120:121], v116 offset:28160
	ds_read_b64_tr_b16 v[122:123], v116 offset:30720
	ds_read_b64_tr_b16 v[124:125], v116 offset:31232
	ds_read_b64_tr_b16 v[114:115], v116 offset:31744
	ds_read_b64_tr_b16 v[116:117], v116 offset:32256
	s_mov_b64 s[36:37], 0
	v_mov_b32_e32 v146, 0
	s_and_saveexec_b64 s[38:39], s[6:7]
	s_cbranch_execz .LBB0_1710
	v_max_f32_e32 v146, v50, v50
	v_max_f32_e32 v147, v34, v34
	v_max_f32_e32 v146, v147, v146
	v_max3_f32 v146, v146, v35, v51
	s_mov_b32 s0, 0x41000000
	v_max3_f32 v146, v146, v36, v52
	s_nop 0
	v_max3_f32 v146, v146, v37, v53
	s_nop 0
	v_max3_f32 v146, v146, v38, v54
	s_nop 0
	v_max3_f32 v146, v146, v39, v55
	s_nop 0
	v_max3_f32 v146, v146, v40, v56
	s_nop 0
	v_max3_f32 v146, v146, v41, v57
	s_nop 0
	v_max3_f32 v146, v146, v42, v58
	s_nop 0
	v_max3_f32 v146, v146, v43, v59
	s_nop 0
	v_max3_f32 v146, v146, v44, v60
	s_nop 0
	v_max3_f32 v146, v146, v45, v61
	s_nop 0
	v_max3_f32 v146, v146, v46, v62
	s_nop 0
	v_max3_f32 v146, v146, v47, v63
	s_nop 0
	v_max3_f32 v146, v146, v48, v64
	s_nop 0
	v_max3_f32 v146, v146, v49, v65
	s_nop 0
	v_mov_b32_e32 v147, v146
	v_mov_b32_e32 v148, v146
	s_nop 1
	v_permlane32_swap_b32_e32 v147, v148
	v_cndmask_b32_e64 v147, v147, v148, s[8:9]
	v_max_f32_e32 v146, v146, v146
	v_max_f32_e32 v147, v147, v147
	v_max_f32_e32 v146, v146, v147
	v_cmp_lt_f32_e32 vcc, s0, v146
	s_cmp_lg_u64 vcc, 0
	s_cselect_b64 s[0:1], -1, 0
	v_max_f32_e32 v146, 0, v146
	s_and_b64 s[36:37], s[0:1], exec
	s_or_b64 exec, exec, s[38:39]
	s_and_saveexec_b64 s[38:39], s[36:37]
	s_cbranch_execnz .LBB0_1711

; #define LDS_WAIT() asm volatile("s_waitcnt lgkmcnt(0)" ::: "memory")
; __device__ __forceinline__ int crow(int r, int hi) { return (r & 3) + 8 * (r >> 2) + 4 * hi; }
; __device__ __forceinline__ void dsa_step(f32x16& c0, f32x16& c1, f32x16& n0, f32x16& n1, const bool have_n, const LAS char* kpn, const LAS char* vpc, const bf16x8 (&qr)[4], unsigned long long mwn, ...
;     ...
;     f32x2 ps2 = {0.f, 0.f};
; #pragma unroll
;     for (int r = 0; r < 16; r += 2) { c0[r] = __builtin_amdgcn_exp2f(c0[r]); c0[r + 1] = __builtin_amdgcn_exp2f(c0[r + 1]); c1[r] = __builtin_amdgcn_exp2f(c1[r]); c1[r + 1] = __builtin_amdgcn_exp2f(c1[r + 1]);
;         ps2 += (f32x2){c0[r], c0[r + 1]}; ps2 += (f32x2){c1[r], c1[r + 1]}; }
;     lsum += ps2[0] + ps2[1];
;     if (resc) { LDS_WAIT();
; #pragma unroll
;         for (int r = 0; r < 16; ++r) { const float f = wsf[crow(r, hi)]; o[0][r] *= f; o[1][r] *= f; } }
;     pv_mma(o, vf, c0, c1);
;     asm volatile("s_waitcnt vmcnt(0) lgkmcnt(0)\n\ts_barrier" ::: "memory");
; __device__ __forceinline__ void dsa_block_unit(int b, int g, int m  , const bf16_t* Q, const bf16_t* K, const bf16_t* V, const unsigned long long* mask, bf16_t* O, LAS char* L, int wid, int lane, float sbound  ) {
;     ...
;         { const int t_ = sc; sc = sn; sn = sn2; sn2 = t_; } mwn = mwn2;
;         if (j + 3 <= jd) { glds16_s(Kw + (size_t)(j + 3) * 64 * 128, kvoff, kdst + sn2); glds16_s(Vw + (size_t)(j + 3) * 64 * 128, vvoff, vdst + sn2); mwn2 = mrow[j + 3]; }
;         dsa_step(pb0, pb1, pa0, pa1, j + 1 < jd, kp0 + sn, vp0 + sc, qr, mwn, o, mref, lsum, wsf, r32, hi, fixed, tblp);
.LBB0_1696:
	s_or_b64 exec, exec, s[34:35]
	v_exp_f32_e32 v34, v34
	v_exp_f32_e32 v35, v35
	v_exp_f32_e32 v36, v36
	v_exp_f32_e32 v37, v37
	v_exp_f32_e32 v38, v38
	v_exp_f32_e32 v39, v39
	v_exp_f32_e32 v40, v40
	v_exp_f32_e32 v41, v41
	v_cvt_pk_bf16_f32 v146, v34, v35
	v_cvt_pk_bf16_f32 v147, v36, v37
	v_cvt_pk_bf16_f32 v148, v38, v39
	v_cvt_pk_bf16_f32 v149, v40, v41
	v_exp_f32_e32 v42, v42
	v_exp_f32_e32 v43, v43
	v_exp_f32_e32 v44, v44
	v_exp_f32_e32 v45, v45
	v_exp_f32_e32 v46, v46
	v_exp_f32_e32 v47, v47
	v_exp_f32_e32 v48, v48
	v_exp_f32_e32 v49, v49
	s_waitcnt lgkmcnt(14)
	v_mfma_f32_32x32x16_bf16 v[2:17], v[146:149], v[142:145], v[2:17]
	v_exp_f32_e32 v50, v50
	v_exp_f32_e32 v51, v51
	v_cvt_pk_bf16_f32 v142, v42, v43
	v_cvt_pk_bf16_f32 v143, v44, v45
	v_cvt_pk_bf16_f32 v144, v46, v47
	v_cvt_pk_bf16_f32 v145, v48, v49
	v_exp_f32_e32 v52, v52
	s_waitcnt lgkmcnt(10)
	v_mfma_f32_32x32x16_bf16 v[18:33], v[146:149], v[138:141], v[18:33]
	v_exp_f32_e32 v53, v53
	v_pk_add_f32 v[186:187], v[34:35], 0 op_sel_hi:[1,0]
	v_exp_f32_e32 v54, v54
	v_pk_add_f32 v[186:187], v[50:51], v[186:187]
	v_exp_f32_e32 v55, v55
	v_exp_f32_e32 v56, v56
	v_exp_f32_e32 v57, v57
	v_mfma_f32_32x32x16_bf16 v[2:17], v[142:145], v[134:137], v[2:17]
	v_add_f32_e64 v134, v186, v36
	v_add_f32_e64 v135, v187, v37
	v_cvt_pk_bf16_f32 v136, v54, v55
	v_add_f32_e64 v134, v52, v134
	v_add_f32_e64 v135, v53, v135
	v_cvt_pk_bf16_f32 v137, v56, v57
	v_pk_add_f32 v[134:135], v[134:135], v[38:39]
	v_exp_f32_e32 v58, v58
	v_pk_add_f32 v[138:139], v[54:55], v[134:135]
	s_waitcnt lgkmcnt(8)
	v_mfma_f32_32x32x16_bf16 v[18:33], v[142:145], v[130:133], v[18:33]
	v_cvt_pk_bf16_f32 v134, v50, v51
	v_cvt_pk_bf16_f32 v135, v52, v53
	v_exp_f32_e32 v59, v59
	v_exp_f32_e32 v60, v60
	v_exp_f32_e32 v61, v61
	v_exp_f32_e32 v62, v62
	v_exp_f32_e32 v63, v63
	v_exp_f32_e32 v64, v64
	v_exp_f32_e32 v65, v65
	s_waitcnt lgkmcnt(6)
	v_mfma_f32_32x32x16_bf16 v[2:17], v[134:137], v[126:129], v[2:17]
	v_cvt_pk_bf16_f32 v126, v58, v59
	v_cvt_pk_bf16_f32 v127, v60, v61
	v_cvt_pk_bf16_f32 v128, v62, v63
	v_cvt_pk_bf16_f32 v129, v64, v65
	v_add_f32_e64 v130, v138, v40
	v_add_f32_e64 v131, v139, v41
	s_waitcnt vmcnt(1) lgkmcnt(0)
	s_barrier
	s_add_i32 s0, s21, s58
	s_waitcnt lgkmcnt(2)
	v_mfma_f32_32x32x16_bf16 v[18:33], v[134:137], v[122:125], v[18:33]
	v_add_f32_e64 v130, v56, v130
	v_add_f32_e64 v131, v57, v131
	s_cmp_eq_u32 s0, 3
	v_add_f32_e64 v122, v130, v42
	v_add_f32_e64 v123, v131, v43
	v_readfirstlane_b32 s36, v0
	v_pk_add_f32 v[122:123], v[58:59], v[122:123]
	v_readfirstlane_b32 s37, v1
	v_pk_add_f32 v[122:123], v[122:123], v[44:45]
	v_mfma_f32_32x32x16_bf16 v[2:17], v[126:129], v[118:121], v[2:17]
	v_add_f32_e64 v122, v60, v122
	v_add_f32_e64 v123, v61, v123
	v_add_f32_e64 v118, v122, v46
	v_add_f32_e64 v119, v123, v47
	v_add_f32_e64 v118, v62, v118
	v_add_f32_e64 v119, v63, v119
	v_pk_add_f32 v[118:119], v[118:119], v[48:49]
	s_waitcnt lgkmcnt(0)
	v_mfma_f32_32x32x16_bf16 v[18:33], v[126:129], v[114:117], v[18:33]
	v_add_f32_e64 v118, v64, v118
	v_add_f32_e64 v119, v65, v119
	v_add_f32_e32 v118, v118, v119
	v_add_f32_e32 v157, v157, v118
	s_cbranch_scc1 .LBB0_1682
	s_cmp_gt_u32 s58, s54
	s_waitcnt vmcnt(0)
	v_mov_b64_e32 v[116:117], v[170:171]
.LBB0_1699:
	s_add_i32 s0, s58, -2
	s_cmp_lt_u32 s0, s54
	s_cselect_b64 s[34:35], -1, 0
	s_cmp_ge_u32 s0, s54
	s_cbranch_scc1 .LBB0_1705
	v_add_u32_e32 v34, s59, v174
	ds_read_b128 v[146:149], v34
	ds_read_b128 v[142:145], v34 offset:512
	ds_read_b128 v[138:141], v34 offset:2048
	ds_read_b128 v[134:137], v34 offset:2560
	ds_read_b128 v[130:133], v34 offset:4096
	ds_read_b128 v[126:129], v34 offset:4608
	ds_read_b128 v[122:125], v34 offset:6144
	ds_read_b128 v[118:121], v34 offset:6656
	v_lshrrev_b32_e32 v115, v176, v170
	v_lshrrev_b32_e32 v114, v176, v171
	s_and_saveexec_b64 s[0:1], s[4:5]
	s_xor_b64 s[36:37], exec, s[0:1]
	s_cbranch_execz .LBB0_1702
	v_lshlrev_b32_e32 v34, 4, v115
	v_lshlrev_b32_e32 v35, 4, v114
	s_add_i32 s0, 0, 0x14800
	v_mov_b32_e32 v206, 0xf0
	v_and_or_b32 v34, v34, v206, s0
	v_and_or_b32 v38, v35, v206, s0
	ds_read_b128 v[34:37], v34
	ds_read_b128 v[50:53], v38
	v_lshrrev_b32_e32 v38, 4, v115
	v_lshrrev_b32_e32 v39, 4, v114
	v_and_or_b32 v38, v38, v206, s0
	v_and_or_b32 v42, v39, v206, s0
	ds_read_b128 v[38:41], v38
	ds_read_b128 v[54:57], v42
	v_lshrrev_b32_e32 v42, 12, v115
	v_lshrrev_b32_e32 v43, 12, v114
	v_and_or_b32 v42, v42, v206, s0
	v_and_or_b32 v46, v43, v206, s0
	ds_read_b128 v[42:45], v42
	ds_read_b128 v[58:61], v46
	v_lshrrev_b32_e32 v46, 20, v115
	v_lshrrev_b32_e32 v47, 20, v114
	v_and_or_b32 v46, v46, v206, s0
	v_and_or_b32 v62, v47, v206, s0
	ds_read_b128 v[46:49], v46
	ds_read_b128 v[62:65], v62

; #define LAS __attribute__((address_space(3)))
; __device__ __forceinline__ float max3f(float a, float b, float c) { float r; asm("v_max3_f32 %0, %1, %2, %3" : "=v"(r) : "v"(a), "v"(b), "v"(c)); return r; }
; __device__ __forceinline__ void dsa_qk(f32x16& p0, f32x16& p1, const LAS char* kp, const bf16x8 (&qr)[4], unsigned long long mw, int hi, float mref, const LAS char* tbl) {
;     ...
; #pragma unroll
;     for (int d0 = 0; d0 < 4; ++d0) {
;         p0 = __builtin_amdgcn_mfma_f32_32x32x16_bf16(kf[2 * d0], qr[d0], p0, 0, 0, 0);
;         p1 = __builtin_amdgcn_mfma_f32_32x32x16_bf16(kf[2 * d0 + 1], qr[d0], p1, 0, 0, 0);
;     }
; }
; __device__ __forceinline__ void dsa_step(f32x16& c0, f32x16& c1, f32x16& n0, f32x16& n1, const bool have_n, const LAS char* kpn, const LAS char* vpc, const bf16x8 (&qr)[4], unsigned long long mwn, ...
;     if (have_n) dsa_qk(n0, n1, kpn, qr, mwn, hi, mref, fixed ? tblp : (const LAS char*)nullptr);
;     bf16x8 vf[8]; pv_load(vf, vpc);
;     __builtin_amdgcn_sched_barrier(0);
;     bool resc = false; float rm = 0.f;
;     if (!fixed) {
;         rm = __builtin_fmaxf(c0[0], c1[0]);
; #pragma unroll
;         for (int r = 1; r < 16; ++r) rm = max3f(rm, c0[r], c1[r]);
;         rm = __builtin_fmaxf(rm, swap_other(rm, hi));
;         resc = __builtin_amdgcn_ballot_w64(rm > DSA_THR) != 0ull;
; __device__ __forceinline__ void dsa_block_unit(int b, int g, int m  , const bf16_t* Q, const bf16_t* K, const bf16_t* V, const unsigned long long* mask, bf16_t* O, LAS char* L, int wid, int lane, float sbound  ) {
;     ...
;         if (j + 3 <= jd) { glds16_s(Kw + (size_t)(j + 3) * 64 * 128, kvoff, kdst + sn2); glds16_s(Vw + (size_t)(j + 3) * 64 * 128, vvoff, vdst + sn2); mwn2 = mrow[j + 3]; }
.LBB0_1704:
	s_or_b64 exec, exec, s[36:37]
	s_waitcnt lgkmcnt(1)
	v_mfma_f32_32x32x16_bf16 v[34:49], v[146:149], v[98:101], v[34:49]
	s_waitcnt lgkmcnt(0)
	v_mfma_f32_32x32x16_bf16 v[50:65], v[142:145], v[98:101], v[50:65]
	v_mfma_f32_32x32x16_bf16 v[34:49], v[138:141], v[102:105], v[34:49]
	v_mfma_f32_32x32x16_bf16 v[50:65], v[134:137], v[102:105], v[50:65]
	v_mfma_f32_32x32x16_bf16 v[34:49], v[130:133], v[106:109], v[34:49]
	v_mfma_f32_32x32x16_bf16 v[50:65], v[126:129], v[106:109], v[50:65]
	v_mfma_f32_32x32x16_bf16 v[34:49], v[122:125], v[110:113], v[34:49]
	v_mfma_f32_32x32x16_bf16 v[50:65], v[118:121], v[110:113], v[50:65]
	s_cmp_gt_u32 s58, s54
	s_cbranch_scc1 .Ldl1_skip
	s_add_u32 s0, s16, s30
	s_addc_u32 s1, s17, s31
	s_add_u32 s0, s0, 0xc000
	s_addc_u32 s1, s1, 0
	s_add_i32 s33, s55, s63
	s_add_u32 s2, s18, s30
	s_addc_u32 s3, s19, s31
	s_add_u32 s2, s2, 0xc000
	s_mov_b32 s101, m0
	s_mov_b32 m0, s33
	s_nop 0
	global_load_lds_dwordx4 v172, s[0:1]
	s_mov_b32 m0, s101
	s_addc_u32 s3, s3, 0
	s_add_i32 s100, s55, s64
	s_mov_b32 s0, m0
	s_mov_b32 m0, s100
	s_nop 0
	global_load_lds_dwordx4 v173, s[2:3]
	s_mov_b32 m0, s0
	global_load_dwordx2 v[116:117], v[168:169], off sc1
.Ldl1_skip:
.LBB0_1705:
	v_add_u32_e32 v114, s57, v175
	ds_read_b64_tr_b16 v[146:147], v114 offset:24576
	ds_read_b64_tr_b16 v[148:149], v114 offset:25088
	ds_read_b64_tr_b16 v[138:139], v114 offset:25600
	ds_read_b64_tr_b16 v[140:141], v114 offset:26112
	ds_read_b64_tr_b16 v[142:143], v114 offset:28672
	ds_read_b64_tr_b16 v[144:145], v114 offset:29184
	ds_read_b64_tr_b16 v[134:135], v114 offset:29696
	ds_read_b64_tr_b16 v[136:137], v114 offset:30208
	ds_read_b64_tr_b16 v[130:131], v114 offset:26624
	ds_read_b64_tr_b16 v[132:133], v114 offset:27136
	ds_read_b64_tr_b16 v[122:123], v114 offset:27648
	ds_read_b64_tr_b16 v[124:125], v114 offset:28160
	ds_read_b64_tr_b16 v[126:127], v114 offset:30720
	ds_read_b64_tr_b16 v[128:129], v114 offset:31232
	ds_read_b64_tr_b16 v[118:119], v114 offset:31744
	ds_read_b64_tr_b16 v[120:121], v114 offset:32256
	s_mov_b64 s[36:37], 0
	v_mov_b32_e32 v114, 0
	s_and_saveexec_b64 s[38:39], s[6:7]
	s_cbranch_execz .LBB0_1716
	v_max_f32_e32 v114, v66, v66
	v_max_f32_e32 v115, v82, v82
	v_max_f32_e32 v114, v115, v114
	v_max3_f32 v114, v114, v83, v67
	s_mov_b32 s0, 0x41000000
	v_max3_f32 v114, v114, v84, v68
	s_nop 0
	v_max3_f32 v114, v114, v85, v69
	s_nop 0
	v_max3_f32 v114, v114, v86, v70
	s_nop 0
	v_max3_f32 v114, v114, v87, v71
	s_nop 0
	v_max3_f32 v114, v114, v88, v72
	s_nop 0
	v_max3_f32 v114, v114, v89, v73
	s_nop 0
	v_max3_f32 v114, v114, v90, v74
	s_nop 0
	v_max3_f32 v114, v114, v91, v75
	s_nop 0
	v_max3_f32 v114, v114, v92, v76
	s_nop 0
	v_max3_f32 v114, v114, v93, v77
	s_nop 0
	v_max3_f32 v114, v114, v94, v78
	s_nop 0
	v_max3_f32 v114, v114, v95, v79
	s_nop 0
	v_max3_f32 v114, v114, v96, v80
	s_nop 0
	v_max3_f32 v114, v114, v97, v81
	s_nop 0
	v_mov_b32_e32 v115, v114
	v_mov_b32_e32 v161, v114
	s_nop 1
	v_permlane32_swap_b32_e32 v115, v161
	v_cndmask_b32_e64 v115, v115, v161, s[8:9]
	v_max_f32_e32 v114, v114, v114
	v_max_f32_e32 v115, v115, v115
	v_max_f32_e32 v114, v114, v115
	v_cmp_lt_f32_e32 vcc, s0, v114
	s_cmp_lg_u64 vcc, 0
	s_cselect_b64 s[0:1], -1, 0
	v_max_f32_e32 v114, 0, v114
	s_and_b64 s[36:37], s[0:1], exec
	s_or_b64 exec, exec, s[38:39]
	s_and_saveexec_b64 s[38:39], s[36:37]
	s_cbranch_execnz .LBB0_1717

; #define LAS __attribute__((address_space(3)))
; __device__ __forceinline__ void dsa_qk(f32x16& p0, f32x16& p1, const LAS char* kp, const bf16x8 (&qr)[4], unsigned long long mw, int hi, float mref, const LAS char* tbl) {
;     bf16x8 kf[8];
; #pragma unroll
;     for (int d0 = 0; d0 < 4; ++d0) { kf[2 * d0] = *(const LAS bf16x8*)(kp + d0 * 2048); kf[2 * d0 + 1] = *(const LAS bf16x8*)(kp + d0 * 2048 + 512); }
;     const unsigned mlo = (unsigned)mw >> (4 * hi), mhi = (unsigned)(mw >> 32) >> (4 * hi), negm = __float_as_uint(-mref);
;     if (tbl) {
; #pragma unroll
;         for (int i = 0; i < 4; ++i) { const u32x4 a = *(const LAS u32x4*)(tbl + ((mlo >> (8 * i)) & 15u) * 16u), b = *(const LAS u32x4*)(tbl + ((mhi >> (8 * i)) & 15u) * 16u);
; #pragma unroll
;             for (int e = 0; e < 4; ++e) { p0[4 * i + e] = __uint_as_float(a[e]); p1[4 * i + e] = __uint_as_float(b[e]); } }
; __device__ __forceinline__ void dsa_block_unit(int b, int g, int m  , const bf16_t* Q, const bf16_t* K, const bf16_t* V, const unsigned long long* mask, bf16_t* O, LAS char* L, int wid, int lane, float sbound  ) {
;     ...
;     for (int j = 0; j <= jd; j += 2) {
;         if (j + 2 <= jd) { glds16_s(Kw + (size_t)(j + 2) * 64 * 128, kvoff, kdst + sn2); glds16_s(Vw + (size_t)(j + 2) * 64 * 128, vvoff, vdst + sn2); mwn2 = mrow[j + 2]; }
.LBB0_1755:
	s_add_i32 s37, s35, -1
	s_mov_b32 s36, s0
	s_cmp_gt_u32 s37, s53
	s_waitcnt vmcnt(0)
	v_mov_b64_e32 v[166:167], v[148:149]
.LBB0_1757:
	s_add_i32 s0, s35, -3
	s_cmp_lt_u32 s0, s53
	s_cselect_b64 s[22:23], -1, 0
	s_cmp_ge_u32 s0, s53
	s_cbranch_scc1 .LBB0_1763
	v_add_u32_e32 v0, s34, v174
	ds_read_b128 v[142:145], v0
	ds_read_b128 v[138:141], v0 offset:512
	ds_read_b128 v[134:137], v0 offset:2048
	ds_read_b128 v[130:133], v0 offset:2560
	ds_read_b128 v[126:129], v0 offset:4096
	ds_read_b128 v[122:125], v0 offset:4608
	ds_read_b128 v[118:121], v0 offset:6144
	ds_read_b128 v[114:117], v0 offset:6656
	v_lshrrev_b32_e32 v148, v176, v148
	v_lshrrev_b32_e32 v0, v176, v149
	s_and_saveexec_b64 s[0:1], s[4:5]
	s_xor_b64 s[24:25], exec, s[0:1]
	s_cbranch_execz .LBB0_1760
	v_lshlrev_b32_e32 v66, 4, v148
	v_lshlrev_b32_e32 v67, 4, v0
	v_lshrrev_b32_e32 v70, 4, v148
	v_lshrrev_b32_e32 v71, 4, v0
	v_lshrrev_b32_e32 v74, 12, v148
	v_lshrrev_b32_e32 v75, 12, v0
	v_lshrrev_b32_e32 v78, 20, v148
	s_add_i32 s0, 0, 0x14800
	v_mov_b32_e32 v206, 0xf0
	v_lshrrev_b32_e32 v0, 20, v0
	v_and_or_b32 v66, v66, v206, s0
	v_and_or_b32 v67, v67, v206, s0
	v_and_or_b32 v70, v70, v206, s0
	v_and_or_b32 v71, v71, v206, s0
	v_and_or_b32 v74, v74, v206, s0
	v_and_or_b32 v75, v75, v206, s0
	v_and_or_b32 v78, v78, v206, s0
	ds_read_b128 v[82:85], v66
	ds_read_b128 v[66:69], v67
	ds_read_b128 v[86:89], v70
	ds_read_b128 v[70:73], v71
	ds_read_b128 v[90:93], v74
	ds_read_b128 v[74:77], v75
	v_and_or_b32 v0, v0, v206, s0
	ds_read_b128 v[94:97], v78
	ds_read_b128 v[78:81], v0

; #define LAS __attribute__((address_space(3)))
; __device__ __forceinline__ float max3f(float a, float b, float c) { float r; asm("v_max3_f32 %0, %1, %2, %3" : "=v"(r) : "v"(a), "v"(b), "v"(c)); return r; }
; __device__ __forceinline__ void dsa_qk(f32x16& p0, f32x16& p1, const LAS char* kp, const bf16x8 (&qr)[4], unsigned long long mw, int hi, float mref, const LAS char* tbl) {
;     ...
; #pragma unroll
;     for (int d0 = 0; d0 < 4; ++d0) {
;         p0 = __builtin_amdgcn_mfma_f32_32x32x16_bf16(kf[2 * d0], qr[d0], p0, 0, 0, 0);
;         p1 = __builtin_amdgcn_mfma_f32_32x32x16_bf16(kf[2 * d0 + 1], qr[d0], p1, 0, 0, 0);
;     }
; }
; __device__ __forceinline__ void dsa_step(f32x16& c0, f32x16& c1, f32x16& n0, f32x16& n1, const bool have_n, const LAS char* kpn, const LAS char* vpc, const bf16x8 (&qr)[4], unsigned long long mwn, ...
;     if (have_n) dsa_qk(n0, n1, kpn, qr, mwn, hi, mref, fixed ? tblp : (const LAS char*)nullptr);
;     bf16x8 vf[8]; pv_load(vf, vpc);
;     __builtin_amdgcn_sched_barrier(0);
;     bool resc = false; float rm = 0.f;
;     if (!fixed) {
;         rm = __builtin_fmaxf(c0[0], c1[0]);
; #pragma unroll
;         for (int r = 1; r < 16; ++r) rm = max3f(rm, c0[r], c1[r]);
;         rm = __builtin_fmaxf(rm, swap_other(rm, hi));
;         resc = __builtin_amdgcn_ballot_w64(rm > DSA_THR) != 0ull;
; __device__ __forceinline__ void dsa_block_unit(int b, int g, int m  , const bf16_t* Q, const bf16_t* K, const bf16_t* V, const unsigned long long* mask, bf16_t* O, LAS char* L, int wid, int lane, float sbound  ) {
;     ...
;         if (j + 2 <= jd) { glds16_s(Kw + (size_t)(j + 2) * 64 * 128, kvoff, kdst + sn2); glds16_s(Vw + (size_t)(j + 2) * 64 * 128, vvoff, vdst + sn2); mwn2 = mrow[j + 2]; }
.LBB0_1762:
	s_or_b64 exec, exec, s[24:25]
	s_waitcnt lgkmcnt(1)
	v_mfma_f32_32x32x16_bf16 v[82:97], v[142:145], v[98:101], v[82:97]
	s_waitcnt lgkmcnt(0)
	v_mfma_f32_32x32x16_bf16 v[66:81], v[138:141], v[98:101], v[66:81]
	v_mfma_f32_32x32x16_bf16 v[82:97], v[134:137], v[102:105], v[82:97]
	v_mfma_f32_32x32x16_bf16 v[66:81], v[130:133], v[102:105], v[66:81]
	v_mfma_f32_32x32x16_bf16 v[82:97], v[126:129], v[106:109], v[82:97]
	v_mfma_f32_32x32x16_bf16 v[66:81], v[122:125], v[106:109], v[66:81]
	v_mfma_f32_32x32x16_bf16 v[82:97], v[118:121], v[110:113], v[82:97]
	v_mfma_f32_32x32x16_bf16 v[66:81], v[114:117], v[110:113], v[66:81]
	s_cmp_gt_u32 s37, s53
	s_cbranch_scc1 .Ldl2_skip
	s_add_u32 s0, s16, s20
	s_addc_u32 s1, s17, s21
	s_add_u32 s0, s0, 0x8000
	s_addc_u32 s1, s1, 0
	s_add_i32 s100, s36, s63
	s_add_u32 s2, s18, s20
	s_addc_u32 s3, s19, s21
	s_add_u32 s2, s2, 0x8000
	s_mov_b32 s24, m0
	s_mov_b32 m0, s100
	s_nop 0
	global_load_lds_dwordx4 v172, s[0:1]
	s_mov_b32 m0, s24
	s_addc_u32 s3, s3, 0
	s_add_i32 s101, s36, s64
	s_mov_b32 s0, m0
	s_mov_b32 m0, s101
	s_nop 0
	global_load_lds_dwordx4 v173, s[2:3]
	s_mov_b32 m0, s0
	global_load_dwordx2 v[166:167], v[146:147], off offset:-8 sc1
.Ldl2_skip:
.LBB0_1763:
	v_add_u32_e32 v0, s31, v175
	ds_read_b64_tr_b16 v[142:143], v0 offset:24576
	ds_read_b64_tr_b16 v[144:145], v0 offset:25088
	ds_read_b64_tr_b16 v[134:135], v0 offset:25600
	ds_read_b64_tr_b16 v[136:137], v0 offset:26112
	ds_read_b64_tr_b16 v[138:139], v0 offset:28672
	ds_read_b64_tr_b16 v[140:141], v0 offset:29184
	ds_read_b64_tr_b16 v[130:131], v0 offset:29696
	ds_read_b64_tr_b16 v[132:133], v0 offset:30208
	ds_read_b64_tr_b16 v[126:127], v0 offset:26624
	ds_read_b64_tr_b16 v[128:129], v0 offset:27136
	ds_read_b64_tr_b16 v[118:119], v0 offset:27648
	ds_read_b64_tr_b16 v[120:121], v0 offset:28160
	ds_read_b64_tr_b16 v[122:123], v0 offset:30720
	ds_read_b64_tr_b16 v[124:125], v0 offset:31232
	ds_read_b64_tr_b16 v[114:115], v0 offset:31744
	ds_read_b64_tr_b16 v[116:117], v0 offset:32256
	s_mov_b64 s[24:25], 0
	v_mov_b32_e32 v0, 0
	s_and_saveexec_b64 s[26:27], s[6:7]
	s_cbranch_execz .LBB0_1781
	v_max_f32_e32 v0, v50, v50
	v_max_f32_e32 v148, v34, v34
	v_max_f32_e32 v0, v148, v0
	v_max3_f32 v0, v0, v35, v51
	s_mov_b32 s0, 0x41000000
	v_max3_f32 v0, v0, v36, v52
	s_nop 0
	v_max3_f32 v0, v0, v37, v53
	s_nop 0
	v_max3_f32 v0, v0, v38, v54
	s_nop 0
	v_max3_f32 v0, v0, v39, v55
	s_nop 0
	v_max3_f32 v0, v0, v40, v56
	s_nop 0
	v_max3_f32 v0, v0, v41, v57
	s_nop 0
	v_max3_f32 v0, v0, v42, v58
	s_nop 0
	v_max3_f32 v0, v0, v43, v59
	s_nop 0
	v_max3_f32 v0, v0, v44, v60
	s_nop 0
	v_max3_f32 v0, v0, v45, v61
	s_nop 0
	v_max3_f32 v0, v0, v46, v62
	s_nop 0
	v_max3_f32 v0, v0, v47, v63
	s_nop 0
	v_max3_f32 v0, v0, v48, v64
	s_nop 0
	v_max3_f32 v0, v0, v49, v65
	s_nop 0
	v_mov_b32_e32 v148, v0
	v_mov_b32_e32 v149, v0
	s_nop 1
	v_permlane32_swap_b32_e32 v148, v149
	v_cndmask_b32_e64 v148, v148, v149, s[8:9]
	v_max_f32_e32 v0, v0, v0
	v_max_f32_e32 v148, v148, v148
	v_max_f32_e32 v0, v0, v148
	v_cmp_lt_f32_e32 vcc, s0, v0
	s_cmp_lg_u64 vcc, 0
	s_cselect_b64 s[0:1], -1, 0
	v_max_f32_e32 v0, 0, v0
	s_and_b64 s[24:25], s[0:1], exec
	s_or_b64 exec, exec, s[26:27]
	s_and_saveexec_b64 s[26:27], s[24:25]
	s_cbranch_execnz .LBB0_1782

; #define LDS_WAIT() asm volatile("s_waitcnt lgkmcnt(0)" ::: "memory")
; __device__ __forceinline__ int crow(int r, int hi) { return (r & 3) + 8 * (r >> 2) + 4 * hi; }
; __device__ __forceinline__ void dsa_step(f32x16& c0, f32x16& c1, f32x16& n0, f32x16& n1, const bool have_n, const LAS char* kpn, const LAS char* vpc, const bf16x8 (&qr)[4], unsigned long long mwn, ...
;     ...
;     f32x2 ps2 = {0.f, 0.f};
; #pragma unroll
;     for (int r = 0; r < 16; r += 2) { c0[r] = __builtin_amdgcn_exp2f(c0[r]); c0[r + 1] = __builtin_amdgcn_exp2f(c0[r + 1]); c1[r] = __builtin_amdgcn_exp2f(c1[r]); c1[r + 1] = __builtin_amdgcn_exp2f(c1[r + 1]);
;         ps2 += (f32x2){c0[r], c0[r + 1]}; ps2 += (f32x2){c1[r], c1[r + 1]}; }
;     lsum += ps2[0] + ps2[1];
;     if (resc) { LDS_WAIT();
; #pragma unroll
;         for (int r = 0; r < 16; ++r) { const float f = wsf[crow(r, hi)]; o[0][r] *= f; o[1][r] *= f; } }
;     pv_mma(o, vf, c0, c1);
;     asm volatile("s_waitcnt vmcnt(0) lgkmcnt(0)\n\ts_barrier" ::: "memory");
; __device__ __forceinline__ void dsa_block_unit(int b, int g, int m  , const bf16_t* Q, const bf16_t* K, const bf16_t* V, const unsigned long long* mask, bf16_t* O, LAS char* L, int wid, int lane, float sbound  ) {
;     ...
;         { const int t_ = sc; sc = sn; sn = sn2; sn2 = t_; } mwn = mwn2;
;         if (j + 3 <= jd) { glds16_s(Kw + (size_t)(j + 3) * 64 * 128, kvoff, kdst + sn2); glds16_s(Vw + (size_t)(j + 3) * 64 * 128, vvoff, vdst + sn2); mwn2 = mrow[j + 3]; }
;         dsa_step(pb0, pb1, pa0, pa1, j + 1 < jd, kp0 + sn, vp0 + sc, qr, mwn, o, mref, lsum, wsf, r32, hi, fixed, tblp);
.LBB0_1767:
	s_or_b64 exec, exec, s[22:23]
	v_exp_f32_e32 v34, v34
	v_exp_f32_e32 v35, v35
	v_exp_f32_e32 v36, v36
	v_exp_f32_e32 v37, v37
	v_exp_f32_e32 v38, v38
	v_exp_f32_e32 v39, v39
	v_exp_f32_e32 v40, v40
	v_exp_f32_e32 v41, v41
	v_cvt_pk_bf16_f32 v186, v34, v35
	v_cvt_pk_bf16_f32 v187, v36, v37
	v_cvt_pk_bf16_f32 v188, v38, v39
	v_cvt_pk_bf16_f32 v189, v40, v41
	v_exp_f32_e32 v42, v42
	v_exp_f32_e32 v43, v43
	v_exp_f32_e32 v44, v44
	v_exp_f32_e32 v45, v45
	v_exp_f32_e32 v46, v46
	v_exp_f32_e32 v47, v47
	v_exp_f32_e32 v48, v48
	v_exp_f32_e32 v49, v49
	s_waitcnt lgkmcnt(14)
	v_mfma_f32_32x32x16_bf16 v[18:33], v[186:189], v[142:145], v[18:33]
	v_exp_f32_e32 v50, v50
	v_exp_f32_e32 v51, v51
	v_cvt_pk_bf16_f32 v142, v42, v43
	v_cvt_pk_bf16_f32 v143, v44, v45
	v_cvt_pk_bf16_f32 v144, v46, v47
	v_cvt_pk_bf16_f32 v145, v48, v49
	v_exp_f32_e32 v52, v52
	s_waitcnt lgkmcnt(10)
	v_mfma_f32_32x32x16_bf16 v[2:17], v[186:189], v[138:141], v[2:17]
	v_exp_f32_e32 v53, v53
	v_pk_add_f32 v[148:149], v[34:35], 0 op_sel_hi:[1,0]
	v_exp_f32_e32 v54, v54
	v_pk_add_f32 v[148:149], v[50:51], v[148:149]
	v_exp_f32_e32 v55, v55
	v_exp_f32_e32 v56, v56
	v_exp_f32_e32 v57, v57
	v_mfma_f32_32x32x16_bf16 v[18:33], v[142:145], v[134:137], v[18:33]
	v_add_f32_e64 v134, v148, v36
	v_add_f32_e64 v135, v149, v37
	v_cvt_pk_bf16_f32 v136, v54, v55
	v_add_f32_e64 v134, v52, v134
	v_add_f32_e64 v135, v53, v135
	v_cvt_pk_bf16_f32 v137, v56, v57
	v_pk_add_f32 v[134:135], v[134:135], v[38:39]
	v_exp_f32_e32 v58, v58
	v_pk_add_f32 v[138:139], v[54:55], v[134:135]
	s_waitcnt lgkmcnt(8)
	v_mfma_f32_32x32x16_bf16 v[2:17], v[142:145], v[130:133], v[2:17]
	v_cvt_pk_bf16_f32 v134, v50, v51
	v_cvt_pk_bf16_f32 v135, v52, v53
	v_exp_f32_e32 v59, v59
	v_exp_f32_e32 v60, v60
	v_exp_f32_e32 v61, v61
	v_exp_f32_e32 v62, v62
	v_exp_f32_e32 v63, v63
	v_exp_f32_e32 v64, v64
	v_exp_f32_e32 v65, v65
	s_waitcnt lgkmcnt(6)
	v_mfma_f32_32x32x16_bf16 v[18:33], v[134:137], v[126:129], v[18:33]
	v_cvt_pk_bf16_f32 v126, v58, v59
	v_cvt_pk_bf16_f32 v127, v60, v61
	v_cvt_pk_bf16_f32 v128, v62, v63
	v_cvt_pk_bf16_f32 v129, v64, v65
	v_add_f32_e64 v130, v138, v40
	v_add_f32_e64 v131, v139, v41
	s_waitcnt vmcnt(1) lgkmcnt(0)
	s_barrier
	s_add_i32 s0, s30, s35
	s_waitcnt lgkmcnt(2)
	v_mfma_f32_32x32x16_bf16 v[2:17], v[134:137], v[122:125], v[2:17]
	v_add_f32_e64 v130, v56, v130
	v_add_f32_e64 v131, v57, v131
	s_cmp_eq_u32 s0, 3
	v_add_f32_e64 v122, v130, v42
	v_add_f32_e64 v123, v131, v43
	v_readfirstlane_b32 s25, v1
	v_pk_add_f32 v[122:123], v[58:59], v[122:123]
	s_nop 0
	v_pk_add_f32 v[122:123], v[122:123], v[44:45]
	v_mfma_f32_32x32x16_bf16 v[18:33], v[126:129], v[118:121], v[18:33]
	v_add_f32_e64 v122, v60, v122
	v_add_f32_e64 v123, v61, v123
	v_add_f32_e64 v118, v122, v46
	v_add_f32_e64 v119, v123, v47
	v_add_f32_e64 v118, v62, v118
	v_add_f32_e64 v119, v63, v119
	v_pk_add_f32 v[118:119], v[118:119], v[48:49]
	s_waitcnt lgkmcnt(0)
	v_mfma_f32_32x32x16_bf16 v[2:17], v[126:129], v[114:117], v[2:17]
	v_add_f32_e64 v118, v64, v118
	v_add_f32_e64 v119, v65, v119
	v_add_f32_e32 v0, v118, v119
	v_add_f32_e32 v157, v157, v0
	v_readfirstlane_b32 s24, v0
	s_cbranch_scc1 .LBB0_1753
	s_cmp_gt_u32 s35, s53
	s_waitcnt vmcnt(0)
	v_mov_b64_e32 v[148:149], v[166:167]
.LBB0_1770:
	s_add_i32 s0, s35, -2
	s_cmp_lt_u32 s0, s53
	s_cselect_b64 s[22:23], -1, 0
	s_cmp_ge_u32 s0, s53
	s_cbranch_scc1 .LBB0_1776
	v_add_u32_e32 v0, s36, v174
	ds_read_b128 v[142:145], v0
	ds_read_b128 v[138:141], v0 offset:512
	ds_read_b128 v[134:137], v0 offset:2048
	ds_read_b128 v[130:133], v0 offset:2560
	ds_read_b128 v[126:129], v0 offset:4096
	ds_read_b128 v[122:125], v0 offset:4608
	ds_read_b128 v[118:121], v0 offset:6144
	ds_read_b128 v[114:117], v0 offset:6656
	v_lshrrev_b32_e32 v161, v176, v166
	v_lshrrev_b32_e32 v0, v176, v167
	s_and_saveexec_b64 s[0:1], s[4:5]
	s_xor_b64 s[24:25], exec, s[0:1]
	s_cbranch_execz .LBB0_1773
	v_lshlrev_b32_e32 v34, 4, v161
	v_lshlrev_b32_e32 v35, 4, v0
	s_add_i32 s0, 0, 0x14800
	v_mov_b32_e32 v206, 0xf0
	v_and_or_b32 v34, v34, v206, s0
	v_and_or_b32 v38, v35, v206, s0
	ds_read_b128 v[34:37], v34
	ds_read_b128 v[50:53], v38
	v_lshrrev_b32_e32 v38, 4, v161
	v_lshrrev_b32_e32 v39, 4, v0
	v_and_or_b32 v38, v38, v206, s0
	v_and_or_b32 v42, v39, v206, s0
	ds_read_b128 v[38:41], v38
	ds_read_b128 v[54:57], v42
	v_lshrrev_b32_e32 v42, 12, v161
	v_lshrrev_b32_e32 v43, 12, v0
	v_and_or_b32 v42, v42, v206, s0
	v_and_or_b32 v46, v43, v206, s0
	ds_read_b128 v[42:45], v42
	ds_read_b128 v[58:61], v46
	v_lshrrev_b32_e32 v46, 20, v161
	v_lshrrev_b32_e32 v0, 20, v0
	v_and_or_b32 v46, v46, v206, s0
	v_and_or_b32 v0, v0, v206, s0
	ds_read_b128 v[46:49], v46
	ds_read_b128 v[62:65], v0

; #define LAS __attribute__((address_space(3)))
; __device__ __forceinline__ float max3f(float a, float b, float c) { float r; asm("v_max3_f32 %0, %1, %2, %3" : "=v"(r) : "v"(a), "v"(b), "v"(c)); return r; }
; __device__ __forceinline__ void dsa_qk(f32x16& p0, f32x16& p1, const LAS char* kp, const bf16x8 (&qr)[4], unsigned long long mw, int hi, float mref, const LAS char* tbl) {
;     ...
; #pragma unroll
;     for (int d0 = 0; d0 < 4; ++d0) {
;         p0 = __builtin_amdgcn_mfma_f32_32x32x16_bf16(kf[2 * d0], qr[d0], p0, 0, 0, 0);
;         p1 = __builtin_amdgcn_mfma_f32_32x32x16_bf16(kf[2 * d0 + 1], qr[d0], p1, 0, 0, 0);
;     }
; }
; __device__ __forceinline__ void dsa_step(f32x16& c0, f32x16& c1, f32x16& n0, f32x16& n1, const bool have_n, const LAS char* kpn, const LAS char* vpc, const bf16x8 (&qr)[4], unsigned long long mwn, ...
;     if (have_n) dsa_qk(n0, n1, kpn, qr, mwn, hi, mref, fixed ? tblp : (const LAS char*)nullptr);
;     bf16x8 vf[8]; pv_load(vf, vpc);
;     __builtin_amdgcn_sched_barrier(0);
;     bool resc = false; float rm = 0.f;
;     if (!fixed) {
;         rm = __builtin_fmaxf(c0[0], c1[0]);
; #pragma unroll
;         for (int r = 1; r < 16; ++r) rm = max3f(rm, c0[r], c1[r]);
;         rm = __builtin_fmaxf(rm, swap_other(rm, hi));
;         resc = __builtin_amdgcn_ballot_w64(rm > DSA_THR) != 0ull;
; __device__ __forceinline__ void dsa_block_unit(int b, int g, int m  , const bf16_t* Q, const bf16_t* K, const bf16_t* V, const unsigned long long* mask, bf16_t* O, LAS char* L, int wid, int lane, float sbound  ) {
;     ...
;         if (j + 3 <= jd) { glds16_s(Kw + (size_t)(j + 3) * 64 * 128, kvoff, kdst + sn2); glds16_s(Vw + (size_t)(j + 3) * 64 * 128, vvoff, vdst + sn2); mwn2 = mrow[j + 3]; }
.LBB0_1775:
	s_or_b64 exec, exec, s[24:25]
	s_waitcnt lgkmcnt(1)
	v_mfma_f32_32x32x16_bf16 v[34:49], v[142:145], v[98:101], v[34:49]
	s_waitcnt lgkmcnt(0)
	v_mfma_f32_32x32x16_bf16 v[50:65], v[138:141], v[98:101], v[50:65]
	v_mfma_f32_32x32x16_bf16 v[34:49], v[134:137], v[102:105], v[34:49]
	v_mfma_f32_32x32x16_bf16 v[50:65], v[130:133], v[102:105], v[50:65]
	v_mfma_f32_32x32x16_bf16 v[34:49], v[126:129], v[106:109], v[34:49]
	v_mfma_f32_32x32x16_bf16 v[50:65], v[122:125], v[106:109], v[50:65]
	v_mfma_f32_32x32x16_bf16 v[34:49], v[118:121], v[110:113], v[34:49]
	v_mfma_f32_32x32x16_bf16 v[50:65], v[114:117], v[110:113], v[50:65]
	s_cmp_gt_u32 s35, s53
	s_cbranch_scc1 .Ldl3_skip
	s_add_u32 s0, s16, s20
	s_addc_u32 s1, s17, s21
	s_add_u32 s0, s0, 0xc000
	s_addc_u32 s1, s1, 0
	s_add_i32 s100, s31, s63
	s_add_u32 s2, s18, s20
	s_addc_u32 s3, s19, s21
	s_add_u32 s2, s2, 0xc000
	s_mov_b32 s24, m0
	s_mov_b32 m0, s100
	s_nop 0
	global_load_lds_dwordx4 v172, s[0:1]
	s_mov_b32 m0, s24
	s_addc_u32 s3, s3, 0
	s_add_i32 s101, s31, s64
	s_mov_b32 s0, m0
	s_mov_b32 m0, s101
	s_nop 0
	global_load_lds_dwordx4 v173, s[2:3]
	s_mov_b32 m0, s0
	global_load_dwordx2 v[148:149], v[146:147], off sc1
.Ldl3_skip:
.LBB0_1776:
	v_add_u32_e32 v0, s34, v175
	ds_read_b64_tr_b16 v[142:143], v0 offset:24576
	ds_read_b64_tr_b16 v[144:145], v0 offset:25088
	ds_read_b64_tr_b16 v[134:135], v0 offset:25600
	ds_read_b64_tr_b16 v[136:137], v0 offset:26112
	ds_read_b64_tr_b16 v[138:139], v0 offset:28672
	ds_read_b64_tr_b16 v[140:141], v0 offset:29184
	ds_read_b64_tr_b16 v[130:131], v0 offset:29696
	ds_read_b64_tr_b16 v[132:133], v0 offset:30208
	ds_read_b64_tr_b16 v[126:127], v0 offset:26624
	ds_read_b64_tr_b16 v[128:129], v0 offset:27136
	ds_read_b64_tr_b16 v[118:119], v0 offset:27648
	ds_read_b64_tr_b16 v[120:121], v0 offset:28160
	ds_read_b64_tr_b16 v[122:123], v0 offset:30720
	ds_read_b64_tr_b16 v[124:125], v0 offset:31232
	ds_read_b64_tr_b16 v[114:115], v0 offset:31744
	ds_read_b64_tr_b16 v[116:117], v0 offset:32256
	s_mov_b64 s[24:25], 0
	v_mov_b32_e32 v0, 0
	s_and_saveexec_b64 s[26:27], s[6:7]
	s_cbranch_execz .LBB0_1787
	v_max_f32_e32 v0, v66, v66
	v_max_f32_e32 v161, v82, v82
	v_max_f32_e32 v0, v161, v0
	v_max3_f32 v0, v0, v83, v67
	s_mov_b32 s0, 0x41000000
	v_max3_f32 v0, v0, v84, v68
	s_nop 0
	v_max3_f32 v0, v0, v85, v69
	s_nop 0
	v_max3_f32 v0, v0, v86, v70
	s_nop 0
	v_max3_f32 v0, v0, v87, v71
	s_nop 0
	v_max3_f32 v0, v0, v88, v72
	s_nop 0
	v_max3_f32 v0, v0, v89, v73
	s_nop 0
	v_max3_f32 v0, v0, v90, v74
	s_nop 0
	v_max3_f32 v0, v0, v91, v75
	s_nop 0
	v_max3_f32 v0, v0, v92, v76
	s_nop 0
	v_max3_f32 v0, v0, v93, v77
	s_nop 0
	v_max3_f32 v0, v0, v94, v78
	s_nop 0
	v_max3_f32 v0, v0, v95, v79
	s_nop 0
	v_max3_f32 v0, v0, v96, v80
	s_nop 0
	v_max3_f32 v0, v0, v97, v81
	s_nop 0
	v_mov_b32_e32 v161, v0
	v_mov_b32_e32 v163, v0
	s_nop 1
	v_permlane32_swap_b32_e32 v161, v163
	v_cndmask_b32_e64 v161, v161, v163, s[8:9]
	v_max_f32_e32 v0, v0, v0
	v_max_f32_e32 v161, v161, v161
	v_max_f32_e32 v0, v0, v161
	v_cmp_lt_f32_e32 vcc, s0, v0
	s_cmp_lg_u64 vcc, 0
	s_cselect_b64 s[0:1], -1, 0
	v_max_f32_e32 v0, 0, v0
	s_and_b64 s[24:25], s[0:1], exec
	s_or_b64 exec, exec, s[26:27]
	s_and_saveexec_b64 s[26:27], s[24:25]
	s_cbranch_execnz .LBB0_1788
